# adds nontemporal hint to the in-proj GEMM epilogue stores (bf16 projections, written once)
# speedup vs baseline: 1.0157x; 1.0092x over previous
.LBB0_265:
	v_lshl_or_b32 v4, s74, 8, v185
	v_ashrrev_i32_e32 v5, 31, v4
	v_lshl_add_u32 v16, s70, 8, v1
	v_mov_b64_e32 v[2:3], s[24:25]
	v_mad_i64_i32 v[6:7], s[68:69], v16, s67, v[2:3]
	v_lshlrev_b64 v[4:5], 1, v[4:5]
	s_nop 15
	v_lshl_add_u64 v[10:11], v[6:7], 0, v[4:5]
	v_pk_fma_f32 v[6:7], v[158:159], s[16:17], 0 op_sel_hi:[1,0,0]
	s_nop 15
	s_nop 15
	s_nop 15
	v_pk_fma_f32 v[8:9], v[160:161], s[16:17], 0 op_sel_hi:[1,0,0]
	v_cvt_pk_bf16_f32 v6, v6, v7
	v_pk_fma_f32 v[12:13], v[156:157], s[16:17], 0 op_sel_hi:[1,0,0]
	v_cvt_pk_bf16_f32 v7, v8, v9
	v_pk_fma_f32 v[14:15], v[154:155], s[16:17], 0 op_sel_hi:[1,0,0]
	s_andn2_b64 vcc, exec, s[26:27]
	v_cvt_pk_bf16_f32 v8, v14, v15
	v_cvt_pk_bf16_f32 v9, v12, v13
	global_store_dwordx4 v[10:11], v[6:9], off nt
	v_pk_fma_f32 v[12:13], v[144:145], s[16:17], 0 op_sel_hi:[1,0,0]
	v_pk_fma_f32 v[14:15], v[142:143], s[16:17], 0 op_sel_hi:[1,0,0]
	v_pk_fma_f32 v[6:7], v[150:151], s[16:17], 0 op_sel_hi:[1,0,0]
	v_pk_fma_f32 v[8:9], v[152:153], s[16:17], 0 op_sel_hi:[1,0,0]
	v_cvt_pk_bf16_f32 v6, v6, v7
	s_mov_b64 s[26:27], -1
	v_cvt_pk_bf16_f32 v7, v8, v9
	v_cvt_pk_bf16_f32 v8, v14, v15
	v_cvt_pk_bf16_f32 v9, v12, v13
	global_store_dwordx4 v[10:11], v[6:9], off offset:256 nt
	v_pk_fma_f32 v[12:13], v[140:141], s[16:17], 0 op_sel_hi:[1,0,0]
	v_pk_fma_f32 v[14:15], v[138:139], s[16:17], 0 op_sel_hi:[1,0,0]
	v_or_b32_e32 v6, 16, v16
	v_mad_i64_i32 v[6:7], s[68:69], v6, s67, v[2:3]
	v_lshl_add_u64 v[10:11], v[6:7], 0, v[4:5]
	v_pk_fma_f32 v[6:7], v[146:147], s[16:17], 0 op_sel_hi:[1,0,0]
	v_pk_fma_f32 v[8:9], v[148:149], s[16:17], 0 op_sel_hi:[1,0,0]
	v_cvt_pk_bf16_f32 v6, v6, v7
	s_nop 0
	v_cvt_pk_bf16_f32 v7, v8, v9
	v_cvt_pk_bf16_f32 v8, v14, v15
	v_cvt_pk_bf16_f32 v9, v12, v13
	global_store_dwordx4 v[10:11], v[6:9], off nt
	v_pk_fma_f32 v[12:13], v[128:129], s[16:17], 0 op_sel_hi:[1,0,0]
	v_pk_fma_f32 v[14:15], v[126:127], s[16:17], 0 op_sel_hi:[1,0,0]
	v_pk_fma_f32 v[6:7], v[134:135], s[16:17], 0 op_sel_hi:[1,0,0]
	v_pk_fma_f32 v[8:9], v[136:137], s[16:17], 0 op_sel_hi:[1,0,0]
	v_cvt_pk_bf16_f32 v6, v6, v7
	s_nop 0
	v_cvt_pk_bf16_f32 v7, v8, v9
	v_cvt_pk_bf16_f32 v8, v14, v15
	v_cvt_pk_bf16_f32 v9, v12, v13
	global_store_dwordx4 v[10:11], v[6:9], off offset:256 nt
	v_pk_fma_f32 v[12:13], v[124:125], s[16:17], 0 op_sel_hi:[1,0,0]
	v_pk_fma_f32 v[14:15], v[122:123], s[16:17], 0 op_sel_hi:[1,0,0]
	v_or_b32_e32 v6, 32, v16
	v_mad_i64_i32 v[6:7], s[68:69], v6, s67, v[2:3]
	v_lshl_add_u64 v[10:11], v[6:7], 0, v[4:5]
	v_pk_fma_f32 v[6:7], v[130:131], s[16:17], 0 op_sel_hi:[1,0,0]
	v_pk_fma_f32 v[8:9], v[132:133], s[16:17], 0 op_sel_hi:[1,0,0]
	v_cvt_pk_bf16_f32 v6, v6, v7
	s_nop 0
	v_cvt_pk_bf16_f32 v7, v8, v9
	v_cvt_pk_bf16_f32 v8, v14, v15
	v_cvt_pk_bf16_f32 v9, v12, v13
	global_store_dwordx4 v[10:11], v[6:9], off nt
	v_pk_fma_f32 v[12:13], v[112:113], s[16:17], 0 op_sel_hi:[1,0,0]
	v_pk_fma_f32 v[14:15], v[110:111], s[16:17], 0 op_sel_hi:[1,0,0]
	v_pk_fma_f32 v[6:7], v[118:119], s[16:17], 0 op_sel_hi:[1,0,0]
	v_pk_fma_f32 v[8:9], v[120:121], s[16:17], 0 op_sel_hi:[1,0,0]
	v_cvt_pk_bf16_f32 v6, v6, v7
	s_nop 0
	v_cvt_pk_bf16_f32 v7, v8, v9
	v_cvt_pk_bf16_f32 v8, v14, v15
	v_cvt_pk_bf16_f32 v9, v12, v13
	global_store_dwordx4 v[10:11], v[6:9], off offset:256 nt
	v_pk_fma_f32 v[12:13], v[108:109], s[16:17], 0 op_sel_hi:[1,0,0]
	v_pk_fma_f32 v[14:15], v[106:107], s[16:17], 0 op_sel_hi:[1,0,0]
	v_or_b32_e32 v6, 48, v16
	v_mad_i64_i32 v[6:7], s[68:69], v6, s67, v[2:3]
	v_lshl_add_u64 v[10:11], v[6:7], 0, v[4:5]
	v_pk_fma_f32 v[6:7], v[114:115], s[16:17], 0 op_sel_hi:[1,0,0]
	v_pk_fma_f32 v[8:9], v[116:117], s[16:17], 0 op_sel_hi:[1,0,0]
	v_cvt_pk_bf16_f32 v6, v6, v7
	s_nop 0
	v_cvt_pk_bf16_f32 v7, v8, v9
	v_cvt_pk_bf16_f32 v8, v14, v15
	v_cvt_pk_bf16_f32 v9, v12, v13
	global_store_dwordx4 v[10:11], v[6:9], off nt
	v_pk_fma_f32 v[12:13], v[100:101], s[16:17], 0 op_sel_hi:[1,0,0]
	v_pk_fma_f32 v[14:15], v[98:99], s[16:17], 0 op_sel_hi:[1,0,0]
	v_pk_fma_f32 v[6:7], v[102:103], s[16:17], 0 op_sel_hi:[1,0,0]
	v_pk_fma_f32 v[8:9], v[104:105], s[16:17], 0 op_sel_hi:[1,0,0]
	v_cvt_pk_bf16_f32 v6, v6, v7
	s_nop 0
	v_cvt_pk_bf16_f32 v7, v8, v9
	v_cvt_pk_bf16_f32 v8, v14, v15
	v_cvt_pk_bf16_f32 v9, v12, v13
	global_store_dwordx4 v[10:11], v[6:9], off offset:256 nt
	v_pk_fma_f32 v[12:13], v[92:93], s[16:17], 0 op_sel_hi:[1,0,0]
	v_pk_fma_f32 v[14:15], v[90:91], s[16:17], 0 op_sel_hi:[1,0,0]
	v_add_u32_e32 v6, 0x80, v16
	v_mad_i64_i32 v[6:7], s[68:69], v6, s67, v[2:3]
	v_lshl_add_u64 v[10:11], v[6:7], 0, v[4:5]
	v_pk_fma_f32 v[6:7], v[94:95], s[16:17], 0 op_sel_hi:[1,0,0]
	v_pk_fma_f32 v[8:9], v[96:97], s[16:17], 0 op_sel_hi:[1,0,0]
	v_cvt_pk_bf16_f32 v6, v6, v7
	s_nop 0
	v_cvt_pk_bf16_f32 v7, v8, v9
	v_cvt_pk_bf16_f32 v8, v14, v15
	v_cvt_pk_bf16_f32 v9, v12, v13
	global_store_dwordx4 v[10:11], v[6:9], off nt
	v_pk_fma_f32 v[12:13], v[80:81], s[16:17], 0 op_sel_hi:[1,0,0]
	v_pk_fma_f32 v[14:15], v[78:79], s[16:17], 0 op_sel_hi:[1,0,0]
	v_pk_fma_f32 v[6:7], v[86:87], s[16:17], 0 op_sel_hi:[1,0,0]
	v_pk_fma_f32 v[8:9], v[88:89], s[16:17], 0 op_sel_hi:[1,0,0]
	v_cvt_pk_bf16_f32 v6, v6, v7
	s_nop 0
	v_cvt_pk_bf16_f32 v7, v8, v9
	v_cvt_pk_bf16_f32 v8, v14, v15
	v_cvt_pk_bf16_f32 v9, v12, v13
	global_store_dwordx4 v[10:11], v[6:9], off offset:256 nt
	v_pk_fma_f32 v[12:13], v[76:77], s[16:17], 0 op_sel_hi:[1,0,0]
	v_pk_fma_f32 v[14:15], v[74:75], s[16:17], 0 op_sel_hi:[1,0,0]
	v_add_u32_e32 v6, 0x90, v16
	v_mad_i64_i32 v[6:7], s[68:69], v6, s67, v[2:3]
	v_lshl_add_u64 v[10:11], v[6:7], 0, v[4:5]
	v_pk_fma_f32 v[6:7], v[82:83], s[16:17], 0 op_sel_hi:[1,0,0]
	v_pk_fma_f32 v[8:9], v[84:85], s[16:17], 0 op_sel_hi:[1,0,0]
	v_cvt_pk_bf16_f32 v6, v6, v7
	s_nop 0
	v_cvt_pk_bf16_f32 v7, v8, v9
	v_cvt_pk_bf16_f32 v8, v14, v15
	v_cvt_pk_bf16_f32 v9, v12, v13
	global_store_dwordx4 v[10:11], v[6:9], off nt
	v_pk_fma_f32 v[12:13], v[64:65], s[16:17], 0 op_sel_hi:[1,0,0]
	v_pk_fma_f32 v[14:15], v[62:63], s[16:17], 0 op_sel_hi:[1,0,0]
	v_pk_fma_f32 v[6:7], v[70:71], s[16:17], 0 op_sel_hi:[1,0,0]
	v_pk_fma_f32 v[8:9], v[72:73], s[16:17], 0 op_sel_hi:[1,0,0]
	v_cvt_pk_bf16_f32 v6, v6, v7
	s_nop 0
	v_cvt_pk_bf16_f32 v7, v8, v9
	v_cvt_pk_bf16_f32 v8, v14, v15
	v_cvt_pk_bf16_f32 v9, v12, v13
	global_store_dwordx4 v[10:11], v[6:9], off offset:256 nt
	v_pk_fma_f32 v[12:13], v[60:61], s[16:17], 0 op_sel_hi:[1,0,0]
	v_pk_fma_f32 v[14:15], v[58:59], s[16:17], 0 op_sel_hi:[1,0,0]
	v_add_u32_e32 v6, 0xa0, v16
	v_mad_i64_i32 v[6:7], s[68:69], v6, s67, v[2:3]
	v_lshl_add_u64 v[10:11], v[6:7], 0, v[4:5]
	v_pk_fma_f32 v[6:7], v[66:67], s[16:17], 0 op_sel_hi:[1,0,0]
	v_pk_fma_f32 v[8:9], v[68:69], s[16:17], 0 op_sel_hi:[1,0,0]
	v_cvt_pk_bf16_f32 v6, v6, v7
	s_nop 0
	v_cvt_pk_bf16_f32 v7, v8, v9
	v_cvt_pk_bf16_f32 v8, v14, v15
	v_cvt_pk_bf16_f32 v9, v12, v13
	global_store_dwordx4 v[10:11], v[6:9], off nt
	v_pk_fma_f32 v[12:13], v[48:49], s[16:17], 0 op_sel_hi:[1,0,0]
	v_pk_fma_f32 v[14:15], v[46:47], s[16:17], 0 op_sel_hi:[1,0,0]
	v_pk_fma_f32 v[6:7], v[54:55], s[16:17], 0 op_sel_hi:[1,0,0]
	v_pk_fma_f32 v[8:9], v[56:57], s[16:17], 0 op_sel_hi:[1,0,0]
	v_cvt_pk_bf16_f32 v6, v6, v7
	s_nop 0
	v_cvt_pk_bf16_f32 v7, v8, v9
	v_cvt_pk_bf16_f32 v8, v14, v15
	v_cvt_pk_bf16_f32 v9, v12, v13
	global_store_dwordx4 v[10:11], v[6:9], off offset:256 nt
	v_pk_fma_f32 v[10:11], v[42:43], s[16:17], 0 op_sel_hi:[1,0,0]
	s_nop 0
	v_add_u32_e32 v6, 0xb0, v16
	v_mad_i64_i32 v[2:3], s[68:69], v6, s67, v[2:3]
	v_lshl_add_u64 v[6:7], v[2:3], 0, v[4:5]
	v_pk_fma_f32 v[4:5], v[52:53], s[16:17], 0 op_sel_hi:[1,0,0]
	v_pk_fma_f32 v[2:3], v[50:51], s[16:17], 0 op_sel_hi:[1,0,0]
	v_pk_fma_f32 v[8:9], v[44:45], s[16:17], 0 op_sel_hi:[1,0,0]
	v_cvt_pk_bf16_f32 v2, v2, v3
	v_cvt_pk_bf16_f32 v3, v4, v5
	v_cvt_pk_bf16_f32 v4, v10, v11
	v_pk_fma_f32 v[10:11], v[34:35], s[16:17], 0 op_sel_hi:[1,0,0]
	v_cvt_pk_bf16_f32 v5, v8, v9
	global_store_dwordx4 v[6:7], v[2:5], off nt
	v_pk_fma_f32 v[8:9], v[36:37], s[16:17], 0 op_sel_hi:[1,0,0]
	s_nop 0
	v_pk_fma_f32 v[4:5], v[40:41], s[16:17], 0 op_sel_hi:[1,0,0]
	v_pk_fma_f32 v[2:3], v[38:39], s[16:17], 0 op_sel_hi:[1,0,0]
	s_nop 0
	v_cvt_pk_bf16_f32 v2, v2, v3
	v_cvt_pk_bf16_f32 v3, v4, v5
	v_cvt_pk_bf16_f32 v4, v10, v11
	v_cvt_pk_bf16_f32 v5, v8, v9
	global_store_dwordx4 v[6:7], v[2:5], off offset:256 nt
	s_cbranch_vccnz .LBB0_250
	s_andn2_b64 vcc, exec, s[6:7]
	s_cbranch_vccnz .LBB0_249
	s_barrier
	s_branch .LBB0_249
